# one static s_setprio 1 for waves 4-7 around the NSA tile loops (reset at loop exit)
# baseline (speedup 1.0000x reference)
; __device__ __forceinline__ void nsa_unit(const Args& a, LAS unsigned char* lds, int b, int kvh, int qb) {
;     ...
;     if (w >= 4) asm volatile("s_barrier" ::: "memory");
; #pragma unroll 1
;     for (int it = 0; it <= nTot; ++it) {
.Lcn_lgo_n0s:
	v_and_b32_e32 v224, 63, v0
	v_and_b32_e32 v253, 7, v224
	v_lshrrev_b32_e32 v224, 3, v224
	v_lshlrev_b32_e32 v224, 2, v224
	v_lshlrev_b32_e32 v225, 4, v253
	v_lshlrev_b32_e32 v253, 2, v253
	v_mad_u32_u24 v254, v224, s65, v225
	global_load_dwordx4 v[212:215], v254, s[32:33] nt
	s_add_u32 s32, s32, s65
	s_addc_u32 s33, s33, 0
	global_load_dwordx4 v[216:219], v254, s[32:33] nt
	s_add_u32 s32, s32, s65
	s_addc_u32 s33, s33, 0
	global_load_dwordx4 v[220:223], v254, s[32:33] nt
	s_add_u32 s32, s32, s65
	s_addc_u32 s33, s33, 0
	global_load_dwordx2 v[224:225], v254, s[32:33] offset:0 nt
	global_load_dword v253, v254, s[32:33] offset:8 nt
	global_load_dword v254, v254, s[32:33] offset:12 nt
	v_readfirstlane_b32 s12, v0
	s_nop 3
	s_lshr_b32 s12, s12, 6
	s_cmp_ge_u32 s12, 4
	s_cbranch_scc0 .Lprio_done_n0
	s_setprio 1
.Lprio_done_n0:
	s_branch .LBB0_897
.LBB0_896:
	s_add_i32 s74, s74, 1
	s_addk_i32 s75, 0x4000
	s_add_i32 s62, s62, 1
	s_cmp_eq_u32 s23, s74
	s_cbranch_scc1 .Lcn_exit_n0

; __device__ __forceinline__ unsigned pk4_fp8(float a, float b, float c, float d) { int p = __builtin_amdgcn_cvt_pk_fp8_f32(a, b, 0, false); p = __builtin_amdgcn_cvt_pk_fp8_f32(c, d, p, true); return (unsigned)p; }
; __device__ __forceinline__ void witem_store(const WItem& w, const f32x4 (&v)[16]) {
;     if (!w.valid) return;
;     if (w.f8) {
; #pragma unroll
;         for (int j = 0; j < 4; ++j) { u32x4 o; const float sc = w.scale;
;             o.x = pk4_fp8(v[0][j] * sc, v[1][j] * sc, v[2][j] * sc, v[3][j] * sc); o.y = pk4_fp8(v[4][j] * sc, v[5][j] * sc, v[6][j] * sc, v[7][j] * sc);
;             o.z = pk4_fp8(v[8][j] * sc, v[9][j] * sc, v[10][j] * sc, v[11][j] * sc); o.w = pk4_fp8(v[12][j] * sc, v[13][j] * sc, v[14][j] * sc, v[15][j] * sc);
;             *(u32x4*)(w.dst + (size_t)witem_row(w.kind, w.n + j) * w.K + w.k0) = o; }
; __device__ __forceinline__ void nsa_unit(const Args& a, LAS unsigned char* lds, int b, int kvh, int qb) {
;     ...
;     }
;     if (w < 4) asm volatile("s_barrier" ::: "memory");
;     __syncthreads();
.Lcn_exit_n0:
	s_setprio 0
	s_bitcmp1_b32 s25, 31
	s_cbranch_scc0 .Lcn_xnone_n0
	s_waitcnt vmcnt(0)
	s_bitcmp1_b32 s25, 31
	s_cbranch_scc0 .Lcn_snone_n0x
	s_and_b32 s12, s25, 0xfffffff
	s_lshr_b32 s12, s12, 2
	s_lshl_b32 s12, s12, 11
	s_add_u32 s12, s12, s100
	s_mov_b32 s13, 0x42000000
	s_cmp_ge_u32 s12, 0xe000
	s_cselect_b32 s13, 0x43000000, s13
	v_mul_f32_e32 v212, s13, v212
	v_mul_f32_e32 v213, s13, v213
	v_mul_f32_e32 v214, s13, v214
	v_mul_f32_e32 v215, s13, v215
	v_mul_f32_e32 v216, s13, v216
	v_mul_f32_e32 v217, s13, v217
	v_mul_f32_e32 v218, s13, v218
	v_mul_f32_e32 v219, s13, v219
	v_mul_f32_e32 v220, s13, v220
	v_mul_f32_e32 v221, s13, v221
	v_mul_f32_e32 v222, s13, v222
	v_mul_f32_e32 v223, s13, v223
	v_mul_f32_e32 v224, s13, v224
	v_mul_f32_e32 v225, s13, v225
	v_mul_f32_e32 v253, s13, v253
	v_mul_f32_e32 v254, s13, v254
	v_cvt_pk_fp8_f32 v212, v212, v216
	v_cvt_pk_fp8_f32 v213, v213, v217
	v_cvt_pk_fp8_f32 v214, v214, v218
	v_cvt_pk_fp8_f32 v215, v215, v219
	v_cvt_pk_fp8_f32 v212, v220, v224 op_sel:[0,0,1]
	v_cvt_pk_fp8_f32 v213, v221, v225 op_sel:[0,0,1]
	v_cvt_pk_fp8_f32 v214, v222, v253 op_sel:[0,0,1]
	v_cvt_pk_fp8_f32 v215, v223, v254 op_sel:[0,0,1]
	s_and_b32 s12, s25, 3
	v_and_b32_e32 v216, 63, v0
	v_and_b32_e32 v217, 7, v216
	v_lshrrev_b32_e32 v216, 3, v216
	v_and_b32_e32 v218, 3, v217
	v_xor_b32_e32 v218, s12, v218
	v_lshlrev_b32_e32 v218, 5, v218
	v_lshl_add_u32 v218, v216, 2, v218
	v_lshl_add_u32 v218, v217, 9, v218
	v_and_b32_e32 v219, 0x1c0, v0
	v_lshl_add_u32 v218, v219, 6, v218
	v_add_u32_e32 v218, 0x1c000, v218
	ds_write_b32 v218, v212 offset:0
	ds_write_b32 v218, v213 offset:128
	ds_write_b32 v218, v214 offset:256
	ds_write_b32 v218, v215 offset:384
	s_mov_b32 s67, s25
	s_mov_b32 s25, 0

; __device__ __forceinline__ void nsa_unit(const Args& a, LAS unsigned char* lds, int b, int kvh, int qb) {
;     ...
;     float mrun = -1e30f, lrun = 0.f;
;     f32x16 p0, p1;
; #pragma unroll
;     for (int i = 0; i < 16; ++i) { p0[i] = 0.f; p1[i] = 0.f; }
;     bf16x8 pf[2][2];
;     if (w >= 4) asm volatile("s_barrier" ::: "memory");
; #pragma unroll 1
;     for (int it = 0; it <= nTot; ++it) {
.Lcn_lgo_n1s:
	v_and_b32_e32 v220, 63, v0
	v_and_b32_e32 v253, 7, v220
	v_lshrrev_b32_e32 v220, 3, v220
	v_lshlrev_b32_e32 v220, 2, v220
	v_lshlrev_b32_e32 v221, 4, v253
	v_lshlrev_b32_e32 v253, 2, v253
	v_mad_u32_u24 v254, v220, vcc_lo, v221
	global_load_dwordx4 v[212:215], v254, s[32:33] nt
	s_add_u32 s32, s32, vcc_lo
	s_addc_u32 s33, s33, 0
	global_load_dwordx4 v[216:219], v254, s[32:33] nt
	s_add_u32 s32, s32, vcc_lo
	s_addc_u32 s33, s33, 0
	global_load_dwordx4 v[224:227], v254, s[32:33] nt
	s_add_u32 s32, s32, vcc_lo
	s_addc_u32 s33, s33, 0
	global_load_dwordx2 v[220:221], v254, s[32:33] offset:0 nt
	global_load_dword v253, v254, s[32:33] offset:8 nt
	global_load_dword v254, v254, s[32:33] offset:12 nt
	v_readfirstlane_b32 s14, v0
	s_nop 3
	s_lshr_b32 s14, s14, 6
	s_cmp_ge_u32 s14, 4
	s_cbranch_scc0 .Lprio_done_n1
	s_setprio 1
.Lprio_done_n1:
	s_branch .LBB0_1843
.LBB0_1842:
	s_add_i32 s70, s70, 1
	s_addk_i32 s71, 0x4000
	s_add_i32 s68, s68, 1
	s_cmp_eq_u32 s56, s70
	s_cbranch_scc1 .Lcn_exit_n1

; __device__ __forceinline__ unsigned pk4_fp8(float a, float b, float c, float d) { int p = __builtin_amdgcn_cvt_pk_fp8_f32(a, b, 0, false); p = __builtin_amdgcn_cvt_pk_fp8_f32(c, d, p, true); return (unsigned)p; }
; __device__ __forceinline__ void witem_store(const WItem& w, const f32x4 (&v)[16]) {
;     ...
;         for (int j = 0; j < 4; ++j) { u32x4 o; const float sc = w.scale;
;             o.x = pk4_fp8(v[0][j] * sc, v[1][j] * sc, v[2][j] * sc, v[3][j] * sc); o.y = pk4_fp8(v[4][j] * sc, v[5][j] * sc, v[6][j] * sc, v[7][j] * sc);
;             o.z = pk4_fp8(v[8][j] * sc, v[9][j] * sc, v[10][j] * sc, v[11][j] * sc); o.w = pk4_fp8(v[12][j] * sc, v[13][j] * sc, v[14][j] * sc, v[15][j] * sc);
;             *(u32x4*)(w.dst + (size_t)witem_row(w.kind, w.n + j) * w.K + w.k0) = o; }
; __device__ __forceinline__ void nsa_unit(const Args& a, LAS unsigned char* lds, int b, int kvh, int qb) {
;     ...
;         if (it < nTot) nsa_qk_sw(lds + (it % 3) * NTB, qf, ro, ho, p0, p1);
;     }
;     if (w < 4) asm volatile("s_barrier" ::: "memory");
;     __syncthreads();
.Lcn_exit_n1:
	s_setprio 0
	s_bitcmp1_b32 s25, 31
	s_cbranch_scc0 .Lcn_xnone_n1
	s_waitcnt vmcnt(0)
	s_bitcmp1_b32 s25, 31
	s_cbranch_scc0 .Lcn_snone_n1x
	s_and_b32 s14, s25, 0xfffffff
	s_lshr_b32 s14, s14, 2
	s_lshl_b32 s14, s14, 11
	s_add_u32 s14, s14, s100
	s_mov_b32 s15, 0x42000000
	s_cmp_ge_u32 s14, 0xe000
	s_cselect_b32 s15, 0x43000000, s15
	v_mul_f32_e32 v212, s15, v212
	v_mul_f32_e32 v213, s15, v213
	v_mul_f32_e32 v214, s15, v214
	v_mul_f32_e32 v215, s15, v215
	v_mul_f32_e32 v216, s15, v216
	v_mul_f32_e32 v217, s15, v217
	v_mul_f32_e32 v218, s15, v218
	v_mul_f32_e32 v219, s15, v219
	v_mul_f32_e32 v224, s15, v224
	v_mul_f32_e32 v225, s15, v225
	v_mul_f32_e32 v226, s15, v226
	v_mul_f32_e32 v227, s15, v227
	v_mul_f32_e32 v220, s15, v220
	v_mul_f32_e32 v221, s15, v221
	v_mul_f32_e32 v253, s15, v253
	v_mul_f32_e32 v254, s15, v254
	v_cvt_pk_fp8_f32 v212, v212, v216
	v_cvt_pk_fp8_f32 v213, v213, v217
	v_cvt_pk_fp8_f32 v214, v214, v218
	v_cvt_pk_fp8_f32 v215, v215, v219
	v_cvt_pk_fp8_f32 v212, v224, v220 op_sel:[0,0,1]
	v_cvt_pk_fp8_f32 v213, v225, v221 op_sel:[0,0,1]
	v_cvt_pk_fp8_f32 v214, v226, v253 op_sel:[0,0,1]
	v_cvt_pk_fp8_f32 v215, v227, v254 op_sel:[0,0,1]
	s_and_b32 s14, s25, 3
	v_and_b32_e32 v216, 63, v0
	v_and_b32_e32 v217, 7, v216
	v_lshrrev_b32_e32 v216, 3, v216
	v_and_b32_e32 v218, 3, v217
	v_xor_b32_e32 v218, s14, v218
	v_lshlrev_b32_e32 v218, 5, v218
	v_lshl_add_u32 v218, v216, 2, v218
	v_lshl_add_u32 v218, v217, 9, v218
	v_and_b32_e32 v219, 0x1c0, v0
	v_lshl_add_u32 v218, v219, 6, v218
	v_add_u32_e32 v218, 0x1c000, v218
	ds_write_b32 v218, v212 offset:0
	ds_write_b32 v218, v213 offset:128
	ds_write_b32 v218, v214 offset:256
	ds_write_b32 v218, v215 offset:384
	s_mov_b32 s67, s25
	s_mov_b32 s25, 0
